# speedup vs baseline: 1.0273x; 1.0106x over previous
.LBB1_10:
	s_add_i32 s20, s33, -1
	s_cmp_eq_u32 s33, 0
	s_cselect_b32 s20, 2, s20
	s_mul_i32 s20, s20, 0x9000
	s_cmp_gt_u32 s18, 39
	s_cselect_b32 s14, s46, 0
	s_cmp_lg_u32 s14, 0
	s_cbranch_scc1 .Lnf_inact
	s_mov_b64 s[14:15], 0
	s_mul_i32 s21, s33, 0x9000
	s_add_i32 s22, s21, 0x8000
	s_and_b32 s19, s18, 7
	v_lshl_add_u32 v130, v207, 4, s22
	s_cmp_lg_u32 s19, 0
	v_lshl_add_u32 v189, v1, 4, v130
	s_cbranch_scc1 .LBB1_15
	ds_read_b128 v[66:69], v189 offset:33280
	ds_read_b128 v[70:73], v189 offset:33312
	ds_read_b128 v[74:77], v189 offset:33344
	ds_read_b128 v[78:81], v189 offset:33376
	ds_read_b128 v[82:85], v189 offset:33408
	ds_read_b128 v[86:89], v189 offset:33440
	ds_read_b128 v[90:93], v189 offset:33472
	ds_read_b128 v[94:97], v189 offset:33504
	ds_read_b128 v[98:101], v189 offset:33536
	ds_read_b128 v[102:105], v189 offset:33568
	ds_read_b128 v[106:109], v189 offset:33600
	ds_read_b128 v[110:113], v189 offset:33632
	ds_read_b128 v[114:117], v189 offset:33664
	ds_read_b128 v[118:121], v189 offset:33696
	ds_read_b128 v[122:125], v189 offset:33728
	ds_read_b128 v[126:129], v189 offset:33760
	s_waitcnt lgkmcnt(12)
	v_mfma_f32_32x32x16_f16 v[66:81], v[178:181], v[146:149], v[66:81]
	s_waitcnt lgkmcnt(8)
	v_mfma_f32_32x32x16_f16 v[82:97], v[178:181], v[154:157], v[82:97]
	s_waitcnt lgkmcnt(4)
	v_mfma_f32_32x32x16_f16 v[98:113], v[178:181], v[162:165], v[98:113]
	s_waitcnt lgkmcnt(0)
	v_mfma_f32_32x32x16_f16 v[114:129], v[178:181], v[170:173], v[114:129]
	v_mfma_f32_32x32x16_f16 v[66:81], v[182:185], v[150:153], v[66:81]
	v_mfma_f32_32x32x16_f16 v[82:97], v[182:185], v[158:161], v[82:97]
	v_mfma_f32_32x32x16_f16 v[98:113], v[182:185], v[166:169], v[98:113]
	v_mfma_f32_32x32x16_f16 v[114:129], v[182:185], v[174:177], v[114:129]

.LBB1_17:
	s_or_b64 exec, exec, s[14:15]
	s_cmpk_eq_i32 s17, 0xa40
	s_cbranch_scc0 .LBB1_9
	s_mov_b64 s[14:15], -1
	s_and_b64 s[20:21], s[6:7], s[14:15]
	s_and_saveexec_b64 s[14:15], s[20:21]
	s_cbranch_execz .LBB1_9
	v_cvt_pk_f16_f32 v133, v8, v9
	v_cvt_pk_f16_f32 v132, v6, v7
	v_cvt_pk_f16_f32 v131, v4, v5
	v_cvt_pk_f16_f32 v130, v2, v3
	ds_write_b128 v223, v[130:133]
	v_cvt_pk_f16_f32 v133, v16, v17
	v_cvt_pk_f16_f32 v132, v14, v15
	v_cvt_pk_f16_f32 v131, v12, v13
	v_cvt_pk_f16_f32 v130, v10, v11
	ds_write_b128 v223, v[130:133] offset:1024
	v_cvt_pk_f16_f32 v133, v56, v57
	v_cvt_pk_f16_f32 v132, v54, v55
	v_cvt_pk_f16_f32 v131, v52, v53
	v_cvt_pk_f16_f32 v130, v50, v51
	ds_write_b128 v223, v[130:133] offset:2048
	v_cvt_pk_f16_f32 v133, v64, v65
	v_cvt_pk_f16_f32 v132, v62, v63
	v_cvt_pk_f16_f32 v131, v60, v61
	v_cvt_pk_f16_f32 v130, v58, v59
	ds_write_b128 v223, v[130:133] offset:3072
	v_cvt_pk_f16_f32 v133, v40, v41
	v_cvt_pk_f16_f32 v132, v38, v39
	v_cvt_pk_f16_f32 v131, v36, v37
	v_cvt_pk_f16_f32 v130, v34, v35
	ds_write_b128 v223, v[130:133] offset:4096
	v_cvt_pk_f16_f32 v133, v48, v49
	v_cvt_pk_f16_f32 v132, v46, v47
	v_cvt_pk_f16_f32 v131, v44, v45
	v_cvt_pk_f16_f32 v130, v42, v43
	ds_write_b128 v223, v[130:133] offset:5120
	v_cvt_pk_f16_f32 v133, v24, v25
	v_cvt_pk_f16_f32 v132, v22, v23
	v_cvt_pk_f16_f32 v131, v20, v21
	v_cvt_pk_f16_f32 v130, v18, v19
	ds_write_b128 v223, v[130:133] offset:6144
	v_cvt_pk_f16_f32 v133, v32, v33
	v_cvt_pk_f16_f32 v132, v30, v31
	v_cvt_pk_f16_f32 v131, v28, v29
	v_cvt_pk_f16_f32 v130, v26, v27
	ds_write_b128 v223, v[130:133] offset:7168
	s_branch .LBB1_9
.Lnf_inact:
	s_add_u32 s22, s12, 0x12000
	v_readfirstlane_b32 s19, v0
	s_addc_u32 s23, s16, 0
	s_lshl_b32 s19, s19, 4
	s_and_b32 s21, s19, 0xfffffc00
	s_add_i32 s21, s21, s20
	s_cmp_lg_u32 s3, -1
	s_cselect_b32 s24, s3, 0
	s_add_i32 s21, s21, s24
	s_mov_b32 m0, s21
	s_nop 0
	global_load_lds_dwordx4 v226, s[22:23]
	s_add_u32 s22, s12, 0x14000
	s_addc_u32 s23, s16, 0
	s_add_i32 s24, s21, 0x2000
	s_mov_b32 m0, s24
	s_nop 0
	global_load_lds_dwordx4 v226, s[22:23]
	s_add_u32 s22, s12, 0x16000
	s_addc_u32 s23, s16, 0
	s_add_i32 s24, s21, 0x4000
	s_mov_b32 m0, s24
	s_nop 0
	global_load_lds_dwordx4 v226, s[22:23]
	s_add_u32 s22, s12, 0x18000
	s_addc_u32 s23, s16, 0
	s_add_i32 s24, s21, 0x6000
	s_mov_b32 m0, s24
	s_nop 0
	global_load_lds_dwordx4 v226, s[22:23]
	s_add_u32 s22, s12, 0x1a000
	s_addc_u32 s23, s16, 0
	s_and_b32 s19, s19, 0xfffff000
	s_sub_i32 s19, s21, s19
	s_add_i32 s19, s19, 0x8000
	s_mov_b32 m0, s19
	s_nop 0
	global_load_lds_dwordx4 v224, s[22:23]
	s_mov_b64 s[14:15], 0
	s_branch .LBB1_17

.LBB1_26:
	s_and_b32 s16, s40, 7
	s_cmp_lg_u32 s16, 0
	s_cbranch_scc1 .LBB1_33
	s_cmp_eq_u32 s40, 32
	s_cselect_b64 s[16:17], -1, 0
	s_and_b64 s[18:19], s[10:11], s[16:17]
	s_and_saveexec_b64 s[16:17], s[18:19]
	s_cbranch_execz .LBB1_28
	s_mov_b64 s[18:19], src_shared_base
	s_cmp_lg_u32 0, -1
	s_cselect_b32 s18, s19, 0
	s_cselect_b32 s19, 0, 0
	v_mov_b32_e32 v66, s19
	v_mov_b32_e32 v67, s18
	flat_store_dword v[66:67], v228 sc0 sc1
	s_waitcnt vmcnt(0)
